# speedup vs baseline: 1.0029x; 1.0029x over previous
_Z7gemm_h3ILi64ELi64ELi0EEvPKDF16_S1_lS1_S1_iPKfPfllPDF16_S5_iifii:
	s_load_dword s3, s[0:1], 0x78
	s_load_dwordx4 s[8:11], s[0:1], 0x0
	s_load_dwordx4 s[12:15], s[0:1], 0x18
	s_waitcnt lgkmcnt(0)
	s_ashr_i32 s4, s3, 3
	s_and_b32 s5, s3, 7
	s_and_b32 s3, s2, 7
	s_add_i32 s6, s4, 1
	s_cmp_ge_u32 s3, s5
	s_cbranch_scc0 .LBB7_2
	s_mul_i32 s7, s6, s5
	s_sub_i32 s5, s3, s5
	s_mul_i32 s5, s5, s4
	s_add_i32 s16, s7, s5
	s_cbranch_execz .LBB7_3
	s_branch .LBB7_4

.LBB7_4:
	s_load_dwordx4 s[4:7], s[0:1], 0x60
	s_load_dword s3, s[0:1], 0x70
	s_ashr_i32 s2, s2, 3
	s_add_i32 s2, s16, s2
	s_abs_i32 s16, s2
	s_waitcnt lgkmcnt(0)
	s_abs_i32 s17, s7
	v_cvt_f32_u32_e32 v1, s17
	s_xor_b32 s18, s2, s7
	s_ashr_i32 s19, s18, 31
	s_sub_i32 s18, 0, s17
	v_rcp_iflag_f32_e32 v1, v1
	v_and_b32_e32 v12, 31, v0
	v_mov_b32_e32 v11, 0
	v_mul_f32_e32 v1, 0x4f7ffffe, v1
	v_cvt_u32_f32_e32 v1, v1
	v_accvgpr_write_b32 a0, 0
	v_accvgpr_write_b32 a1, 0
	v_accvgpr_write_b32 a2, 0
	v_readfirstlane_b32 s20, v1
	s_mul_i32 s18, s18, s20
	s_mul_hi_u32 s18, s20, s18
	s_add_i32 s20, s20, s18
	s_mul_hi_u32 s18, s16, s20
	s_mul_i32 s20, s18, s17
	s_sub_i32 s16, s16, s20
	s_add_i32 s21, s18, 1
	s_sub_i32 s20, s16, s17
	s_cmp_ge_u32 s16, s17
	s_cselect_b32 s18, s21, s18
	s_cselect_b32 s16, s20, s16
	s_add_i32 s20, s18, 1
	s_cmp_ge_u32 s16, s17
	s_cselect_b32 s16, s20, s18
	s_abs_i32 s18, s3
	v_cvt_f32_u32_e32 v1, s18
	s_xor_b32 s16, s16, s19
	s_sub_i32 s19, s16, s19
	s_mul_i32 s16, s19, s7
	v_rcp_iflag_f32_e32 v1, v1
	s_sub_i32 s17, 0, s18
	s_sub_i32 s2, s2, s16
	s_lshl_b32 s2, s2, 6
	v_mul_f32_e32 v1, 0x4f7ffffe, v1
	v_cvt_u32_f32_e32 v1, v1
	s_abs_i32 s21, s19
	s_ashr_i32 s20, s3, 31
	s_ashr_i32 s7, s19, 31
	v_readfirstlane_b32 s16, v1
	v_lshrrev_b32_e32 v1, 1, v0
	s_mul_i32 s17, s17, s16
	v_and_b32_e32 v1, 32, v1
	s_mul_hi_u32 s17, s16, s17
	v_or_b32_e32 v15, v1, v12
	s_add_i32 s16, s16, s17
	v_or_b32_e32 v2, s2, v15
	s_mul_hi_u32 s22, s21, s16
	v_cmp_gt_i32_e32 vcc, s4, v2
	v_accvgpr_write_b32 a3, 0
	v_accvgpr_write_b32 a4, 0
	v_accvgpr_write_b32 a5, 0
	v_accvgpr_write_b32 a6, 0
	v_accvgpr_write_b32 a7, 0
	v_accvgpr_write_b32 a8, 0
	v_accvgpr_write_b32 a9, 0
	v_accvgpr_write_b32 a10, 0
	v_accvgpr_write_b32 a11, 0
	v_accvgpr_write_b32 a12, 0
	v_accvgpr_write_b32 a13, 0
	v_accvgpr_write_b32 a14, 0
	v_accvgpr_write_b32 a15, 0
	v_mov_b32_e32 v13, 0
	s_and_saveexec_b64 s[16:17], vcc
	s_cbranch_execz .LBB7_6
	s_load_dwordx2 s[24:25], s[0:1], 0x30
	v_ashrrev_i32_e32 v3, 31, v2
	s_waitcnt lgkmcnt(0)
	v_lshl_add_u64 v[2:3], v[2:3], 2, s[24:25]
	global_load_dword v13, v[2:3], off

_Z7gemm_h3ILi64ELi64ELi1EEvPKDF16_S1_lS1_S1_iPKfPfllPDF16_S5_iifii:
	s_load_dword s4, s[0:1], 0x78
	s_load_dwordx4 s[8:11], s[0:1], 0x0
	s_load_dwordx4 s[12:15], s[0:1], 0x18
	s_and_b32 s6, s2, 7
	s_waitcnt lgkmcnt(0)
	s_ashr_i32 s3, s4, 3
	s_and_b32 s4, s4, 7
	s_add_i32 s7, s3, 1
	s_cmp_ge_u32 s6, s4
	s_cbranch_scc0 .LBB11_2
	s_mul_i32 s5, s7, s4
	s_sub_i32 s4, s6, s4
	s_mul_i32 s4, s4, s3
	s_add_i32 s3, s5, s4
	s_cbranch_execz .LBB11_3
	s_branch .LBB11_4
.LBB11_2:
.LBB11_3:
	s_mul_i32 s3, s7, s6
.LBB11_4:
	s_load_dwordx4 s[4:7], s[0:1], 0x60
	s_load_dword s16, s[0:1], 0x70
	s_ashr_i32 s2, s2, 3
	s_add_i32 s18, s3, s2
	s_abs_i32 s2, s18
	s_waitcnt lgkmcnt(0)
	s_abs_i32 s17, s7
	v_cvt_f32_u32_e32 v1, s17
	s_xor_b32 s3, s18, s7
	s_ashr_i32 s19, s3, 31
	s_sub_i32 s3, 0, s17
	v_rcp_iflag_f32_e32 v1, v1
	v_lshrrev_b32_e32 v13, 2, v0
	v_mov_b32_e32 v31, 0
	v_lshrrev_b32_e32 v10, 1, v0
	v_mul_f32_e32 v1, 0x4f7ffffe, v1
	v_cvt_u32_f32_e32 v1, v1
	v_and_b32_e32 v11, 32, v13
	v_accvgpr_write_b32 a0, 0
	v_accvgpr_write_b32 a1, 0
	v_readfirstlane_b32 s20, v1
	s_mul_i32 s3, s3, s20
	s_mul_hi_u32 s3, s20, s3
	s_add_i32 s20, s20, s3
	s_mul_hi_u32 s3, s2, s20
	s_mul_i32 s20, s3, s17
	s_sub_i32 s2, s2, s20
	s_add_i32 s21, s3, 1
	s_sub_i32 s20, s2, s17
	s_cmp_ge_u32 s2, s17
	s_cselect_b32 s3, s21, s3
	s_cselect_b32 s2, s20, s2
	s_add_i32 s20, s3, 1
	s_cmp_ge_u32 s2, s17
	s_cselect_b32 s17, s20, s3
	s_abs_i32 s20, s16
	v_cvt_f32_u32_e32 v1, s20
	s_xor_b32 s17, s17, s19
	s_sub_i32 s19, s17, s19
	s_mul_i32 s7, s19, s7
	v_rcp_iflag_f32_e32 v1, v1
	s_xor_b32 s17, s19, s16
	s_sub_i32 s22, 0, s20
	s_sub_i32 s18, s18, s7
	v_mul_f32_e32 v1, 0x4f7ffffe, v1
	v_cvt_u32_f32_e32 v1, v1
	s_ashr_i32 s7, s17, 31
	s_abs_i32 s23, s19
	s_load_dwordx2 s[2:3], s[0:1], 0x10
	s_load_dword s21, s[0:1], 0x28
	v_readfirstlane_b32 s17, v1
	s_mul_i32 s22, s22, s17
	s_mul_hi_u32 s22, s17, s22
	s_add_i32 s17, s17, s22
	s_mul_hi_u32 s17, s23, s17
	s_mul_i32 s22, s17, s20
	s_sub_i32 s22, s23, s22
	s_add_i32 s24, s17, 1
	s_sub_i32 s23, s22, s20
	s_cmp_ge_u32 s22, s20
	s_cselect_b32 s17, s24, s17
	s_cselect_b32 s22, s23, s22
	s_add_i32 s23, s17, 1
	s_cmp_ge_u32 s22, s20
	s_cselect_b32 s17, s23, s17
	s_xor_b32 s17, s17, s7
	s_sub_i32 s17, s17, s7
	s_mul_i32 s7, s17, s16
	s_lshl_b32 s16, s18, 6
	v_lshlrev_b32_e32 v1, 3, v0
	s_mul_i32 s18, s17, s5
	s_sub_i32 s7, s19, s7
	v_and_b32_e32 v30, 24, v1
	s_ashr_i32 s19, s18, 31
	s_lshl_b32 s7, s7, 6
	v_lshl_add_u64 v[2:3], s[18:19], 0, v[30:31]
	v_or_b32_e32 v4, s16, v13
	s_add_i32 s18, s4, -1
	v_or_b32_e32 v1, s7, v13
	s_ashr_i32 s20, s7, 31
	v_min_i32_e32 v6, s18, v4
	s_waitcnt lgkmcnt(0)
	s_mul_i32 s20, s2, s20
	v_mad_u64_u32 v[4:5], s[18:19], s2, v1, v[2:3]
	v_mul_lo_u32 v1, s3, v1
	v_mad_i64_i32 v[6:7], s[2:3], v6, s21, v[2:3]
	v_add3_u32 v5, v1, v5, s20
	v_lshlrev_b64 v[6:7], 1, v[6:7]
	v_lshlrev_b64 v[8:9], 1, v[4:5]
	v_lshl_add_u64 v[4:5], s[12:13], 0, v[6:7]
	global_load_dwordx4 v[64:67], v[4:5], off
	v_lshl_add_u64 v[6:7], s[14:15], 0, v[6:7]
	v_lshl_add_u64 v[2:3], s[8:9], 0, v[8:9]
	global_load_dwordx4 v[68:71], v[6:7], off
	global_load_dwordx4 v[72:75], v[2:3], off
	v_lshl_add_u64 v[8:9], s[10:11], 0, v[8:9]
	global_load_dwordx4 v[76:79], v[8:9], off
	s_load_dwordx2 s[8:9], s[0:1], 0x38
	v_mul_u32_u24_e32 v13, 40, v13
	v_lshlrev_b32_e32 v30, 1, v30
	s_mov_b32 s2, 0
	v_and_b32_e32 v1, 31, v0
	v_accvgpr_write_b32 a2, 0
	v_accvgpr_write_b32 a3, 0
	v_accvgpr_write_b32 a4, 0
	v_accvgpr_write_b32 a5, 0
	v_accvgpr_write_b32 a6, 0
	v_accvgpr_write_b32 a7, 0
	v_accvgpr_write_b32 a8, 0
	v_accvgpr_write_b32 a9, 0
	v_accvgpr_write_b32 a10, 0
	v_accvgpr_write_b32 a11, 0
	v_accvgpr_write_b32 a12, 0
	v_accvgpr_write_b32 a13, 0
	v_accvgpr_write_b32 a14, 0
	v_accvgpr_write_b32 a15, 0
	v_bfe_u32 v12, v0, 5, 1
	v_and_b32_e32 v10, 32, v10
	v_lshl_add_u32 v13, v13, 1, v30
	s_ashr_i32 s3, s5, 31
	s_lshr_b32 s3, s3, 27
	s_add_i32 s3, s5, s3
	s_ashr_i32 s3, s3, 5
	s_add_i32 s5, s3, -1
	s_min_i32 s10, s5, 2
	s_lshl_b32 s10, s10, 5
	s_ashr_i32 s11, s10, 31
	s_lshl_b64 s[10:11], s[10:11], 1
	v_lshl_add_u64 v[14:15], v[2:3], 0, s[10:11]
	global_load_dwordx4 v[16:19], v[2:3], off offset:64
	global_load_dwordx4 v[20:23], v[8:9], off offset:64
	global_load_dwordx4 v[24:27], v[4:5], off offset:64
	global_load_dwordx4 v[32:35], v[6:7], off offset:64
	global_load_dwordx4 v[28:31], v[14:15], off
	v_lshl_add_u64 v[14:15], v[8:9], 0, s[10:11]
	global_load_dwordx4 v[36:39], v[14:15], off
	v_lshl_add_u64 v[14:15], v[4:5], 0, s[10:11]
	global_load_dwordx4 v[40:43], v[14:15], off
	v_lshl_add_u64 v[14:15], v[6:7], 0, s[10:11]
	global_load_dwordx4 v[44:47], v[14:15], off
	s_waitcnt vmcnt(11)
	ds_write_b128 v13, v[64:67] offset:10240
	s_waitcnt vmcnt(10)
	ds_write_b128 v13, v[68:71] offset:15360
	s_waitcnt vmcnt(9)
	ds_write_b128 v13, v[72:75]
	s_waitcnt vmcnt(8)
	ds_write_b128 v13, v[76:79] offset:5120
	s_waitcnt lgkmcnt(0)
	s_barrier
	v_or_b32_e32 v15, v10, v1
	v_lshlrev_b32_e32 v64, 4, v12
	s_movk_i32 s10, 0x50
	v_or_b32_e32 v14, v11, v1
	v_mul_u32_u24_e32 v65, 0x50, v15
	v_mad_u32_u24 v15, v15, s10, v64
	v_mul_u32_u24_e32 v66, 0x50, v14
	v_mad_u32_u24 v14, v14, s10, v64
	ds_read_b128 v[56:59], v15 offset:15360
	ds_read_b128 v[48:51], v15 offset:10240
	ds_read_b128 v[52:55], v14
	ds_read_b128 v[60:63], v14 offset:5120
	v_accvgpr_write_b32 a15, 0
	v_accvgpr_write_b32 a14, 0
	v_accvgpr_write_b32 a13, 0
	v_accvgpr_write_b32 a12, 0
	v_accvgpr_write_b32 a11, 0
	v_accvgpr_write_b32 a10, 0
	v_accvgpr_write_b32 a9, 0
	v_accvgpr_write_b32 a8, 0
	v_accvgpr_write_b32 a7, 0
	v_accvgpr_write_b32 a6, 0
	v_accvgpr_write_b32 a5, 0
	v_accvgpr_write_b32 a4, 0
	v_accvgpr_write_b32 a3, 0
	v_accvgpr_write_b32 a2, 0
	v_accvgpr_write_b32 a1, 0
	v_accvgpr_write_b32 a0, 0
	v_add_u32_e32 v14, v64, v66
	v_add_u32_e32 v15, v64, v65

.LBB11_9:
	s_endpgm
	s_endpgm
	s_endpgm
	s_endpgm
	s_endpgm
	s_endpgm
	s_endpgm
	s_endpgm
	s_endpgm
	s_endpgm
	s_endpgm
	s_endpgm
	s_endpgm
	s_endpgm
	s_endpgm
	s_endpgm
	s_endpgm
	s_endpgm
	s_endpgm
	s_endpgm
	s_endpgm
	s_endpgm
	s_endpgm
	.section	.rodata,"a",@progbits
	.p2align	6, 0x0

_Z7gemm_h3ILi64ELi64ELi2EEvPKDF16_S1_lS1_S1_iPKfPfllPDF16_S5_iifii:
	s_load_dword s4, s[0:1], 0x78
	s_load_dwordx4 s[8:11], s[0:1], 0x0
	s_load_dwordx4 s[12:15], s[0:1], 0x18
	s_and_b32 s6, s2, 7
	s_waitcnt lgkmcnt(0)
	s_ashr_i32 s3, s4, 3
	s_and_b32 s4, s4, 7
	s_add_i32 s7, s3, 1
	s_cmp_ge_u32 s6, s4
	s_cbranch_scc0 .LBB18_2
	s_mul_i32 s5, s7, s4
	s_sub_i32 s4, s6, s4
	s_mul_i32 s4, s4, s3
	s_add_i32 s3, s5, s4
	s_cbranch_execz .LBB18_3
	s_branch .LBB18_4

.LBB18_4:
	s_load_dwordx4 s[4:7], s[0:1], 0x60
	s_load_dword s16, s[0:1], 0x70
	s_ashr_i32 s2, s2, 3
	s_add_i32 s2, s3, s2
	s_abs_i32 s3, s2
	s_waitcnt lgkmcnt(0)
	s_abs_i32 s17, s7
	v_cvt_f32_u32_e32 v1, s17
	s_sub_i32 s19, 0, s17
	s_xor_b32 s18, s2, s7
	s_ashr_i32 s18, s18, 31
	v_rcp_iflag_f32_e32 v1, v1
	v_and_b32_e32 v13, 31, v0
	v_mov_b32_e32 v3, 0
	v_mul_f32_e32 v1, 0x4f7ffffe, v1
	v_cvt_u32_f32_e32 v1, v1
	v_accvgpr_write_b32 a0, 0
	v_accvgpr_write_b32 a1, 0
	v_accvgpr_write_b32 a2, 0
	v_readfirstlane_b32 s20, v1
	s_mul_i32 s19, s19, s20
	s_mul_hi_u32 s19, s20, s19
	s_add_i32 s20, s20, s19
	s_mul_hi_u32 s19, s3, s20
	s_mul_i32 s20, s19, s17
	s_sub_i32 s3, s3, s20
	s_add_i32 s21, s19, 1
	s_sub_i32 s20, s3, s17
	s_cmp_ge_u32 s3, s17
	s_cselect_b32 s19, s21, s19
	s_cselect_b32 s3, s20, s3
	s_add_i32 s20, s19, 1
	s_cmp_ge_u32 s3, s17
	s_cselect_b32 s3, s20, s19
	s_abs_i32 s17, s16
	v_cvt_f32_u32_e32 v1, s17
	s_xor_b32 s3, s3, s18
	s_sub_i32 s18, s3, s18
	s_mul_i32 s3, s18, s7
	v_rcp_iflag_f32_e32 v1, v1
	s_sub_i32 s2, s2, s3
	s_sub_i32 s22, 0, s17
	s_lshl_b32 s7, s2, 6
	v_mul_f32_e32 v1, 0x4f7ffffe, v1
	v_cvt_u32_f32_e32 v1, v1
	s_abs_i32 s21, s18
	s_ashr_i32 s19, s16, 31
	s_ashr_i32 s20, s18, 31
	v_readfirstlane_b32 s2, v1
	v_lshrrev_b32_e32 v1, 1, v0
	s_mul_i32 s22, s22, s2
	v_and_b32_e32 v1, 32, v1
	s_mul_hi_u32 s3, s2, s22
	v_or_b32_e32 v16, v1, v13
	s_add_i32 s2, s2, s3
	v_or_b32_e32 v4, s7, v16
	s_mul_hi_u32 s22, s21, s2
	v_cmp_gt_i32_e32 vcc, s4, v4
	v_accvgpr_write_b32 a3, 0
	v_accvgpr_write_b32 a4, 0
	v_accvgpr_write_b32 a5, 0
	v_accvgpr_write_b32 a6, 0
	v_accvgpr_write_b32 a7, 0
	v_accvgpr_write_b32 a8, 0
	v_accvgpr_write_b32 a9, 0
	v_accvgpr_write_b32 a10, 0
	v_accvgpr_write_b32 a11, 0
	v_accvgpr_write_b32 a12, 0
	v_accvgpr_write_b32 a13, 0
	v_accvgpr_write_b32 a14, 0
	v_accvgpr_write_b32 a15, 0
	v_mov_b32_e32 v12, 0
	s_and_saveexec_b64 s[2:3], vcc
	s_cbranch_execz .LBB18_6
	s_load_dwordx2 s[24:25], s[0:1], 0x30
	v_ashrrev_i32_e32 v5, 31, v4
	s_waitcnt lgkmcnt(0)
	v_lshl_add_u64 v[4:5], v[4:5], 2, s[24:25]
	global_load_dword v12, v[4:5], off
